# grid barrier: every workgroup writes back its L2 before signalling arrival (instead of one write-back by the last arriver of each XCD on the critical path)
# baseline (speedup 1.0000x reference)
.LBB0_127:
	s_lshl_b32 s0, s33, 8
	s_add_u32 s21, s34, s0
	s_addc_u32 s20, s35, 0
	v_mov_b32_e32 v1, s21
	v_add_co_u32_e32 v6, vcc, 0x1000, v1
	v_mov_b32_e32 v1, s20
	s_nop 0
	v_addc_co_u32_e32 v7, vcc, 0, v1, vcc
	v_mov_b32_e32 v1, 1
	buffer_wbl2 sc1
	s_waitcnt vmcnt(0)
	flat_atomic_add v1, v[6:7], v1 offset:1024 sc0
	v_cvt_f32_u32_e32 v3, v4
	v_sub_u32_e32 v5, 0, v4
	v_rcp_iflag_f32_e32 v3, v3
	s_nop 0
	v_mul_f32_e32 v3, 0x4f7ffffe, v3
	v_cvt_u32_f32_e32 v3, v3
	v_mul_lo_u32 v5, v5, v3
	v_mul_hi_u32 v5, v3, v5
	v_add_u32_e32 v3, v3, v5
	s_waitcnt vmcnt(0) lgkmcnt(0)
	v_mul_hi_u32 v3, v1, v3
	v_mul_lo_u32 v5, v3, v4
	v_add_u32_e32 v6, 1, v1
	v_sub_u32_e32 v1, v1, v5
	v_add_u32_e32 v7, 1, v3
	v_cmp_ge_u32_e32 vcc, v1, v4
	v_sub_u32_e32 v5, v1, v4
	s_nop 0
	v_cndmask_b32_e32 v3, v3, v7, vcc
	v_cndmask_b32_e32 v1, v1, v5, vcc
	v_add_u32_e32 v5, 1, v3
	v_cmp_ge_u32_e32 vcc, v1, v4
	s_nop 1
	v_cndmask_b32_e32 v1, v3, v5, vcc
	v_mad_u64_u32 v[4:5], s[0:1], v4, v1, v[4:5]
	v_cmp_ne_u32_e32 vcc, v6, v4
	s_and_saveexec_b64 s[0:1], vcc
	s_xor_b64 s[0:1], exec, s[0:1]
	s_cbranch_execz .LBB0_140
	v_mov_b32_e32 v2, s21
	v_add_co_u32_e32 v2, vcc, 0x2000, v2
	v_mov_b32_e32 v3, s20
	s_nop 0
	v_addc_co_u32_e32 v3, vcc, 0, v3, vcc
	flat_load_dword v2, v[2:3] offset:1024 sc1
	s_add_u32 s4, s21, 0x2400
	s_addc_u32 s5, s20, 0
	s_waitcnt vmcnt(0) lgkmcnt(0)
	v_cmp_eq_u32_e32 vcc, v2, v1
	s_and_saveexec_b64 s[2:3], vcc
	s_cbranch_execz .LBB0_139
	s_mov_b32 s22, 1
	s_mov_b64 s[6:7], 0
	s_branch .LBB0_131

.LBB0_140:
	s_andn2_saveexec_b64 s[0:1], s[0:1]
	s_cbranch_execz .LBB0_156
	v_mov_b32_e32 v1, s34
	v_add_co_u32_e32 v4, vcc, 0x3000, v1
	v_mov_b32_e32 v1, s35
	v_addc_co_u32_e32 v5, vcc, 0, v1, vcc
	v_mov_b32_e32 v1, 1
	flat_atomic_add v1, v[4:5], v1 offset:1024 sc0
	v_cvt_f32_u32_e32 v3, v2
	v_sub_u32_e32 v4, 0, v2
	s_add_u32 s0, s34, 0x3500
	s_addc_u32 s1, s35, 0
	v_rcp_iflag_f32_e32 v3, v3
	s_mov_b64 s[4:5], -1
	v_mul_f32_e32 v3, 0x4f7ffffe, v3
	v_cvt_u32_f32_e32 v3, v3
	v_mul_lo_u32 v4, v4, v3
	v_mul_hi_u32 v4, v3, v4
	v_add_u32_e32 v3, v3, v4
	s_waitcnt vmcnt(0) lgkmcnt(0)
	v_mul_hi_u32 v3, v1, v3
	v_mul_lo_u32 v5, v3, v2
	v_add_u32_e32 v4, 1, v1
	v_sub_u32_e32 v1, v1, v5
	v_add_u32_e32 v6, 1, v3
	v_cmp_ge_u32_e32 vcc, v1, v2
	v_sub_u32_e32 v5, v1, v2
	s_nop 0
	v_cndmask_b32_e32 v3, v3, v6, vcc
	v_cndmask_b32_e32 v1, v1, v5, vcc
	v_add_u32_e32 v5, 1, v3
	v_cmp_ge_u32_e32 vcc, v1, v2
	s_nop 1
	v_cndmask_b32_e32 v1, v3, v5, vcc
	v_mad_u64_u32 v[2:3], s[2:3], v2, v1, v[2:3]
	v_cmp_ne_u32_e32 vcc, v4, v2
	v_mov_b64_e32 v[2:3], s[0:1]
	s_and_saveexec_b64 s[2:3], vcc
	s_cbranch_execz .LBB0_153
	v_mov_b64_e32 v[2:3], s[0:1]
	flat_load_dword v2, v[2:3] sc1
	s_mov_b64 s[8:9], 0
	s_waitcnt vmcnt(0) lgkmcnt(0)
	v_cmp_eq_u32_e32 vcc, v2, v1
	s_and_saveexec_b64 s[6:7], vcc
	s_cbranch_execz .LBB0_152
	s_add_u32 s4, s34, 0x200
	s_addc_u32 s5, s35, 0
	s_mov_b32 s22, 1
	s_branch .LBB0_145

.LBB0_193:
	v_readlane_b32 s4, v251, 48
	s_lshl_b32 s4, s4, 2
	s_add_u32 s25, s2, s4
	s_addc_u32 s24, s3, 0
	v_mov_b32_e32 v1, s25
	v_add_co_u32_e32 v8, vcc, 0x1000, v1
	v_mov_b32_e32 v1, s24
	s_nop 0
	v_addc_co_u32_e32 v9, vcc, 0, v1, vcc
	buffer_wbl2 sc1
	s_waitcnt vmcnt(0)
	flat_atomic_add v1, v[8:9], v211 offset:1024 sc0
	v_cvt_f32_u32_e32 v3, v6
	v_sub_u32_e32 v5, 0, v6
	v_rcp_iflag_f32_e32 v3, v3
	s_nop 0
	v_mul_f32_e32 v3, 0x4f7ffffe, v3
	v_cvt_u32_f32_e32 v3, v3
	v_mul_lo_u32 v5, v5, v3
	v_mul_hi_u32 v5, v3, v5
	v_add_u32_e32 v3, v3, v5
	s_waitcnt vmcnt(0) lgkmcnt(0)
	v_mul_hi_u32 v3, v1, v3
	v_mul_lo_u32 v7, v3, v6
	v_add_u32_e32 v5, 1, v1
	v_sub_u32_e32 v1, v1, v7
	v_add_u32_e32 v8, 1, v3
	v_cmp_ge_u32_e32 vcc, v1, v6
	v_sub_u32_e32 v7, v1, v6
	s_nop 0
	v_cndmask_b32_e32 v3, v3, v8, vcc
	v_cndmask_b32_e32 v1, v1, v7, vcc
	v_add_u32_e32 v7, 1, v3
	v_cmp_ge_u32_e32 vcc, v1, v6
	s_nop 1
	v_cndmask_b32_e32 v1, v3, v7, vcc
	v_mad_u64_u32 v[6:7], s[4:5], v6, v1, v[6:7]
	v_cmp_ne_u32_e32 vcc, v5, v6
	s_and_saveexec_b64 s[4:5], vcc
	s_xor_b64 s[4:5], exec, s[4:5]
	s_cbranch_execz .LBB0_206
	v_mov_b32_e32 v3, s25
	v_add_co_u32_e32 v4, vcc, 0x2000, v3
	v_mov_b32_e32 v3, s24
	s_nop 0
	v_addc_co_u32_e32 v5, vcc, 0, v3, vcc
	flat_load_dword v3, v[4:5] offset:1024 sc1
	s_add_u32 s8, s25, 0x2400
	s_addc_u32 s9, s24, 0
	s_waitcnt vmcnt(0) lgkmcnt(0)
	v_cmp_eq_u32_e32 vcc, v3, v1
	s_and_saveexec_b64 s[6:7], vcc
	s_cbranch_execz .LBB0_205
	s_mov_b32 s26, 1
	s_mov_b64 s[10:11], 0
	s_branch .LBB0_197

.LBB0_206:
	s_andn2_saveexec_b64 s[4:5], s[4:5]
	s_cbranch_execz .LBB0_222
	v_mov_b32_e32 v1, s2
	v_add_co_u32_e32 v6, vcc, 0x3000, v1
	v_mov_b32_e32 v1, s3
	v_addc_co_u32_e32 v7, vcc, 0, v1, vcc
	flat_atomic_add v1, v[6:7], v211 offset:1024 sc0
	v_cvt_f32_u32_e32 v3, v4
	v_sub_u32_e32 v5, 0, v4
	s_add_u32 s4, s2, 0x3500
	s_addc_u32 s5, s3, 0
	v_rcp_iflag_f32_e32 v3, v3
	s_mov_b64 s[8:9], -1
	v_mul_f32_e32 v3, 0x4f7ffffe, v3
	v_cvt_u32_f32_e32 v3, v3
	v_mul_lo_u32 v5, v5, v3
	v_mul_hi_u32 v5, v3, v5
	v_add_u32_e32 v3, v3, v5
	s_waitcnt vmcnt(0) lgkmcnt(0)
	v_mul_hi_u32 v3, v1, v3
	v_mul_lo_u32 v5, v3, v4
	v_add_u32_e32 v6, 1, v1
	v_sub_u32_e32 v1, v1, v5
	v_add_u32_e32 v7, 1, v3
	v_cmp_ge_u32_e32 vcc, v1, v4
	v_sub_u32_e32 v5, v1, v4
	s_nop 0
	v_cndmask_b32_e32 v3, v3, v7, vcc
	v_cndmask_b32_e32 v1, v1, v5, vcc
	v_add_u32_e32 v5, 1, v3
	v_cmp_ge_u32_e32 vcc, v1, v4
	s_nop 1
	v_cndmask_b32_e32 v1, v3, v5, vcc
	v_mad_u64_u32 v[4:5], s[6:7], v4, v1, v[4:5]
	v_cmp_ne_u32_e32 vcc, v6, v4
	v_mov_b64_e32 v[4:5], s[4:5]
	s_and_saveexec_b64 s[6:7], vcc
	s_cbranch_execz .LBB0_219
	v_mov_b64_e32 v[4:5], s[4:5]
	flat_load_dword v3, v[4:5] sc1
	s_mov_b64 s[12:13], 0
	s_waitcnt vmcnt(0) lgkmcnt(0)
	v_cmp_eq_u32_e32 vcc, v3, v1
	s_and_saveexec_b64 s[10:11], vcc
	s_cbranch_execz .LBB0_218
	s_add_u32 s8, s2, 0x200
	s_addc_u32 s9, s3, 0
	s_mov_b32 s22, 1
	s_mov_b64 s[2:3], 0
	s_branch .LBB0_211

.LBB0_360:
	v_readlane_b32 s4, v251, 48
	s_lshl_b32 s4, s4, 2
	s_add_u32 s25, s2, s4
	s_addc_u32 s24, s3, 0
	v_mov_b32_e32 v1, s25
	v_add_co_u32_e32 v8, vcc, 0x1000, v1
	v_mov_b32_e32 v1, s24
	s_nop 0
	v_addc_co_u32_e32 v9, vcc, 0, v1, vcc
	buffer_wbl2 sc1
	s_waitcnt vmcnt(0)
	flat_atomic_add v3, v[8:9], v211 offset:1024 sc0
	v_cvt_f32_u32_e32 v1, v6
	v_sub_u32_e32 v5, 0, v6
	v_rcp_iflag_f32_e32 v1, v1
	s_nop 0
	v_mul_f32_e32 v1, 0x4f7ffffe, v1
	v_cvt_u32_f32_e32 v1, v1
	v_mul_lo_u32 v5, v5, v1
	v_mul_hi_u32 v5, v1, v5
	v_add_u32_e32 v1, v1, v5
	s_waitcnt vmcnt(0) lgkmcnt(0)
	v_mul_hi_u32 v1, v3, v1
	v_mul_lo_u32 v5, v1, v6
	v_sub_u32_e32 v5, v3, v5
	v_cmp_ge_u32_e32 vcc, v5, v6
	v_add_u32_e32 v7, 1, v1
	v_add_u32_e32 v3, 1, v3
	v_cndmask_b32_e32 v1, v1, v7, vcc
	v_sub_u32_e32 v7, v5, v6
	v_cndmask_b32_e32 v5, v5, v7, vcc
	v_cmp_ge_u32_e32 vcc, v5, v6
	v_add_u32_e32 v5, 1, v1
	s_nop 0
	v_cndmask_b32_e32 v1, v1, v5, vcc
	v_mad_u64_u32 v[6:7], s[4:5], v6, v1, v[6:7]
	v_cmp_ne_u32_e32 vcc, v3, v6
	s_and_saveexec_b64 s[4:5], vcc
	s_xor_b64 s[4:5], exec, s[4:5]
	s_cbranch_execz .LBB0_373
	v_mov_b32_e32 v3, s25
	v_add_co_u32_e32 v4, vcc, 0x2000, v3
	v_mov_b32_e32 v3, s24
	s_nop 0
	v_addc_co_u32_e32 v5, vcc, 0, v3, vcc
	flat_load_dword v3, v[4:5] offset:1024 sc1
	s_add_u32 s8, s25, 0x2400
	s_addc_u32 s9, s24, 0
	s_waitcnt vmcnt(0) lgkmcnt(0)
	v_cmp_eq_u32_e32 vcc, v3, v1
	s_and_saveexec_b64 s[6:7], vcc
	s_cbranch_execz .LBB0_372
	s_mov_b32 s26, 1
	s_mov_b64 s[10:11], 0
	s_branch .LBB0_364

.LBB0_373:
	s_andn2_saveexec_b64 s[4:5], s[4:5]
	s_cbranch_execz .LBB0_389
	v_mov_b32_e32 v1, s2
	v_add_co_u32_e32 v6, vcc, 0x3000, v1
	v_mov_b32_e32 v1, s3
	v_addc_co_u32_e32 v7, vcc, 0, v1, vcc
	flat_atomic_add v3, v[6:7], v211 offset:1024 sc0
	v_cvt_f32_u32_e32 v1, v4
	v_sub_u32_e32 v5, 0, v4
	s_mov_b64 s[8:9], -1
	v_rcp_iflag_f32_e32 v1, v1
	s_nop 0
	v_mul_f32_e32 v1, 0x4f7ffffe, v1
	v_cvt_u32_f32_e32 v1, v1
	v_mul_lo_u32 v5, v5, v1
	v_mul_hi_u32 v5, v1, v5
	v_add_u32_e32 v1, v1, v5
	s_waitcnt vmcnt(0) lgkmcnt(0)
	v_mul_hi_u32 v1, v3, v1
	v_mul_lo_u32 v5, v1, v4
	v_sub_u32_e32 v5, v3, v5
	v_cmp_ge_u32_e32 vcc, v5, v4
	v_add_u32_e32 v6, 1, v1
	v_add_u32_e32 v3, 1, v3
	v_cndmask_b32_e32 v1, v1, v6, vcc
	v_sub_u32_e32 v6, v5, v4
	v_cndmask_b32_e32 v5, v5, v6, vcc
	v_cmp_ge_u32_e32 vcc, v5, v4
	v_add_u32_e32 v5, 1, v1
	s_nop 0
	v_cndmask_b32_e32 v1, v1, v5, vcc
	v_mad_u64_u32 v[4:5], s[4:5], v4, v1, v[4:5]
	s_add_u32 s4, s2, 0x3500
	s_addc_u32 s5, s3, 0
	v_cmp_ne_u32_e32 vcc, v3, v4
	v_mov_b64_e32 v[4:5], s[4:5]
	s_and_saveexec_b64 s[6:7], vcc
	s_cbranch_execz .LBB0_386
	v_mov_b64_e32 v[4:5], s[4:5]
	flat_load_dword v3, v[4:5] sc1
	s_mov_b64 s[12:13], 0
	s_waitcnt vmcnt(0) lgkmcnt(0)
	v_cmp_eq_u32_e32 vcc, v3, v1
	s_and_saveexec_b64 s[10:11], vcc
	s_cbranch_execz .LBB0_385
	s_add_u32 s8, s2, 0x200
	s_addc_u32 s9, s3, 0
	s_mov_b32 s22, 1
	s_mov_b64 s[2:3], 0
	s_branch .LBB0_378

.LBB0_1326:
	v_mov_b32_e32 v1, s2
	v_add_co_u32_e32 v6, vcc, 0x3000, v1
	v_mov_b32_e32 v1, s3
	v_addc_co_u32_e32 v7, vcc, 0, v1, vcc
	flat_atomic_add v3, v[6:7], v211 offset:1024 sc0
	v_cvt_f32_u32_e32 v1, v4
	v_sub_u32_e32 v5, 0, v4
	s_mov_b64 s[8:9], -1
	v_rcp_iflag_f32_e32 v1, v1
	s_nop 0
	v_mul_f32_e32 v1, 0x4f7ffffe, v1
	v_cvt_u32_f32_e32 v1, v1
	v_mul_lo_u32 v5, v5, v1
	v_mul_hi_u32 v5, v1, v5
	v_add_u32_e32 v1, v1, v5
	s_waitcnt vmcnt(0) lgkmcnt(0)
	v_mul_hi_u32 v1, v3, v1
	v_mul_lo_u32 v5, v1, v4
	v_sub_u32_e32 v5, v3, v5
	v_cmp_ge_u32_e32 vcc, v5, v4
	v_add_u32_e32 v6, 1, v1
	v_add_u32_e32 v3, 1, v3
	v_cndmask_b32_e32 v1, v1, v6, vcc
	v_sub_u32_e32 v6, v5, v4
	v_cndmask_b32_e32 v5, v5, v6, vcc
	v_cmp_ge_u32_e32 vcc, v5, v4
	v_add_u32_e32 v5, 1, v1
	s_nop 0
	v_cndmask_b32_e32 v1, v1, v5, vcc
	v_mad_u64_u32 v[4:5], s[4:5], v4, v1, v[4:5]
	s_add_u32 s4, s2, 0x3500
	s_addc_u32 s5, s3, 0
	v_cmp_ne_u32_e32 vcc, v3, v4
	v_mov_b64_e32 v[4:5], s[4:5]
	s_and_saveexec_b64 s[6:7], vcc
	s_cbranch_execz .LBB0_1338
	v_mov_b64_e32 v[4:5], s[4:5]
	flat_load_dword v3, v[4:5] sc1
	s_mov_b64 s[12:13], 0
	s_waitcnt vmcnt(0) lgkmcnt(0)
	v_cmp_eq_u32_e32 vcc, v3, v1
	s_and_saveexec_b64 s[10:11], vcc
	s_cbranch_execz .LBB0_1337
	s_add_u32 s8, s2, 0x200
	s_addc_u32 s9, s3, 0
	s_mov_b32 s22, 1
	s_mov_b64 s[2:3], 0
	s_branch .LBB0_1330
